# v23 + grid-barrier XCD leaders wait on the cross-XCD arrival counter reaching the round's target instead of on the release-generation word
# speedup vs baseline: 1.0068x; 1.0024x over previous
.LBB0_104:
	s_or_b64 exec, exec, s[38:39]
	s_waitcnt vmcnt(0)
	v_readfirstlane_b32 s4, v3
	v_sub_u32_e32 v4, 0, v2
	s_mov_b64 s[38:39], -1
	v_add_u32_e32 v3, s4, v1
	v_cvt_f32_u32_e32 v1, v2
	v_readlane_b32 s4, v254, 49
	v_readlane_b32 s5, v254, 50
	v_rcp_iflag_f32_e32 v1, v1
	s_nop 0
	v_mul_f32_e32 v1, 0x4f7ffffe, v1
	v_cvt_u32_f32_e32 v1, v1
	v_mul_lo_u32 v4, v4, v1
	v_mul_hi_u32 v4, v1, v4
	v_add_u32_e32 v1, v1, v4
	v_mul_hi_u32 v1, v3, v1
	v_mul_lo_u32 v4, v1, v2
	v_sub_u32_e32 v4, v3, v4
	v_cmp_ge_u32_e32 vcc, v4, v2
	v_add_u32_e32 v5, 1, v1
	v_add_u32_e32 v3, 1, v3
	v_cndmask_b32_e32 v1, v1, v5, vcc
	v_sub_u32_e32 v5, v4, v2
	v_cndmask_b32_e32 v4, v4, v5, vcc
	v_cmp_ge_u32_e32 vcc, v4, v2
	v_add_u32_e32 v4, 1, v1
	s_nop 0
	v_cndmask_b32_e32 v1, v1, v4, vcc
	v_mul_lo_u32 v4, v2, v1
	v_add_u32_e32 v2, v4, v2
	v_mov_b32_e32 v250, v2
	v_cmp_ne_u32_e32 vcc, v3, v2
	v_mov_b64_e32 v[2:3], s[4:5]
	s_and_saveexec_b64 s[28:29], vcc
	s_cbranch_execz .LBB0_116
	v_readlane_b32 s4, v254, 47
	v_readlane_b32 s5, v254, 48
	s_mov_b64 s[40:41], 0
	s_nop 3
	global_load_dword v2, v115, s[4:5] sc1
	s_waitcnt vmcnt(0)
	v_cmp_lt_u32_e32 vcc, v2, v250
	s_and_saveexec_b64 s[38:39], vcc
	s_cbranch_execz .LBB0_115
	s_mov_b32 s4, 1
	s_branch .LBB0_108

.LBB0_110:
	v_readlane_b32 s8, v254, 47
	v_readlane_b32 s9, v254, 48
	s_add_i32 s4, s4, 1
	s_mov_b64 s[46:47], -1
	s_nop 2
	global_load_dword v2, v115, s[8:9] sc1
	s_waitcnt vmcnt(0)
	v_cmp_ge_u32_e32 vcc, v2, v250
	s_orn2_b64 s[44:45], vcc, exec
	s_branch .LBB0_107

.LBB0_255:
	s_or_b64 exec, exec, s[28:29]
	s_waitcnt vmcnt(0)
	v_readfirstlane_b32 s4, v3
	v_sub_u32_e32 v4, 0, v2
	s_mov_b64 s[28:29], -1
	v_add_u32_e32 v3, s4, v1
	v_cvt_f32_u32_e32 v1, v2
	v_readlane_b32 s4, v254, 49
	v_readlane_b32 s5, v254, 50
	v_rcp_iflag_f32_e32 v1, v1
	s_nop 0
	v_mul_f32_e32 v1, 0x4f7ffffe, v1
	v_cvt_u32_f32_e32 v1, v1
	v_mul_lo_u32 v4, v4, v1
	v_mul_hi_u32 v4, v1, v4
	v_add_u32_e32 v1, v1, v4
	v_mul_hi_u32 v1, v3, v1
	v_mul_lo_u32 v4, v1, v2
	v_sub_u32_e32 v4, v3, v4
	v_cmp_ge_u32_e32 vcc, v4, v2
	v_add_u32_e32 v5, 1, v1
	v_add_u32_e32 v3, 1, v3
	v_cndmask_b32_e32 v1, v1, v5, vcc
	v_sub_u32_e32 v5, v4, v2
	v_cndmask_b32_e32 v4, v4, v5, vcc
	v_cmp_ge_u32_e32 vcc, v4, v2
	v_add_u32_e32 v4, 1, v1
	s_nop 0
	v_cndmask_b32_e32 v1, v1, v4, vcc
	v_mul_lo_u32 v4, v2, v1
	v_add_u32_e32 v2, v4, v2
	v_mov_b32_e32 v250, v2
	v_cmp_ne_u32_e32 vcc, v3, v2
	v_mov_b64_e32 v[2:3], s[4:5]
	s_and_saveexec_b64 s[26:27], vcc
	s_cbranch_execz .LBB0_267
	v_readlane_b32 s4, v254, 47
	v_readlane_b32 s5, v254, 48
	s_mov_b64 s[38:39], 0
	s_nop 3
	global_load_dword v2, v115, s[4:5] sc1
	s_waitcnt vmcnt(0)
	v_cmp_lt_u32_e32 vcc, v2, v250
	s_and_saveexec_b64 s[28:29], vcc
	s_cbranch_execz .LBB0_266
	s_mov_b32 s4, 1
	s_branch .LBB0_259

.LBB0_261:
	v_readlane_b32 s8, v254, 47
	v_readlane_b32 s9, v254, 48
	s_add_i32 s4, s4, 1
	s_mov_b64 s[44:45], -1
	s_nop 2
	global_load_dword v2, v115, s[8:9] sc1
	s_waitcnt vmcnt(0)
	v_cmp_ge_u32_e32 vcc, v2, v250
	s_orn2_b64 s[42:43], vcc, exec
	s_branch .LBB0_258

.LBB0_430:
	s_or_b64 exec, exec, s[26:27]
	v_cvt_f32_u32_e32 v4, v2
	s_waitcnt vmcnt(0)
	v_readfirstlane_b32 s4, v3
	s_mov_b64 s[26:27], -1
	v_rcp_iflag_f32_e32 v4, v4
	v_add_u32_e32 v1, s4, v1
	v_add_u32_e32 v5, 1, v1
	v_readlane_b32 s4, v254, 49
	v_mul_f32_e32 v3, 0x4f7ffffe, v4
	v_cvt_u32_f32_e32 v3, v3
	v_sub_u32_e32 v4, 0, v2
	v_readlane_b32 s5, v254, 50
	v_mul_lo_u32 v4, v4, v3
	v_mul_hi_u32 v4, v3, v4
	v_add_u32_e32 v3, v3, v4
	v_mul_hi_u32 v3, v1, v3
	v_mul_lo_u32 v4, v3, v2
	v_sub_u32_e32 v1, v1, v4
	v_add_u32_e32 v6, 1, v3
	v_cmp_ge_u32_e32 vcc, v1, v2
	v_sub_u32_e32 v4, v1, v2
	s_nop 0
	v_cndmask_b32_e32 v3, v3, v6, vcc
	v_cndmask_b32_e32 v1, v1, v4, vcc
	v_add_u32_e32 v4, 1, v3
	v_cmp_ge_u32_e32 vcc, v1, v2
	s_nop 1
	v_cndmask_b32_e32 v1, v3, v4, vcc
	v_mul_lo_u32 v3, v2, v1
	v_add_u32_e32 v2, v3, v2
	v_mov_b32_e32 v250, v2
	v_cmp_ne_u32_e32 vcc, v5, v2
	v_mov_b64_e32 v[2:3], s[4:5]
	s_and_saveexec_b64 s[10:11], vcc
	s_cbranch_execz .LBB0_442
	v_readlane_b32 s4, v254, 47
	v_readlane_b32 s5, v254, 48
	s_mov_b64 s[28:29], 0
	s_nop 3
	global_load_dword v2, v115, s[4:5] sc1
	s_waitcnt vmcnt(0)
	v_cmp_lt_u32_e32 vcc, v2, v250
	s_and_saveexec_b64 s[26:27], vcc
	s_cbranch_execz .LBB0_441
	s_mov_b32 s4, 1
	s_branch .LBB0_434

.LBB0_436:
	v_readlane_b32 s8, v254, 47
	v_readlane_b32 s9, v254, 48
	s_add_i32 s4, s4, 1
	s_mov_b64 s[42:43], -1
	s_nop 2
	global_load_dword v2, v115, s[8:9] sc1
	s_waitcnt vmcnt(0)
	v_cmp_ge_u32_e32 vcc, v2, v250
	s_orn2_b64 s[40:41], vcc, exec
	s_branch .LBB0_433

.LBB0_586:
	s_or_b64 exec, exec, s[28:29]
	s_waitcnt vmcnt(0)
	v_readfirstlane_b32 s4, v3
	v_sub_u32_e32 v4, 0, v2
	s_mov_b64 s[28:29], -1
	v_add_u32_e32 v3, s4, v1
	v_cvt_f32_u32_e32 v1, v2
	v_readlane_b32 s4, v254, 49
	v_readlane_b32 s5, v254, 50
	v_rcp_iflag_f32_e32 v1, v1
	s_nop 0
	v_mul_f32_e32 v1, 0x4f7ffffe, v1
	v_cvt_u32_f32_e32 v1, v1
	v_mul_lo_u32 v4, v4, v1
	v_mul_hi_u32 v4, v1, v4
	v_add_u32_e32 v1, v1, v4
	v_mul_hi_u32 v1, v3, v1
	v_mul_lo_u32 v4, v1, v2
	v_sub_u32_e32 v4, v3, v4
	v_cmp_ge_u32_e32 vcc, v4, v2
	v_add_u32_e32 v5, 1, v1
	v_add_u32_e32 v3, 1, v3
	v_cndmask_b32_e32 v1, v1, v5, vcc
	v_sub_u32_e32 v5, v4, v2
	v_cndmask_b32_e32 v4, v4, v5, vcc
	v_cmp_ge_u32_e32 vcc, v4, v2
	v_add_u32_e32 v4, 1, v1
	s_nop 0
	v_cndmask_b32_e32 v1, v1, v4, vcc
	v_mul_lo_u32 v4, v2, v1
	v_add_u32_e32 v2, v4, v2
	v_mov_b32_e32 v250, v2
	v_cmp_ne_u32_e32 vcc, v3, v2
	v_mov_b64_e32 v[2:3], s[4:5]
	s_and_saveexec_b64 s[10:11], vcc
	s_cbranch_execz .LBB0_598
	v_readlane_b32 s4, v254, 47
	v_readlane_b32 s5, v254, 48
	s_mov_b64 s[38:39], 0
	s_nop 3
	global_load_dword v2, v115, s[4:5] sc1
	s_waitcnt vmcnt(0)
	v_cmp_lt_u32_e32 vcc, v2, v250
	s_and_saveexec_b64 s[28:29], vcc
	s_cbranch_execz .LBB0_597
	s_mov_b32 s4, 1
	s_branch .LBB0_590

.LBB0_1038:
	s_or_b64 exec, exec, s[8:9]
	s_waitcnt vmcnt(0)
	v_readfirstlane_b32 s4, v3
	v_sub_u32_e32 v4, 0, v2
	s_mov_b64 s[8:9], -1
	v_add_u32_e32 v3, s4, v1
	v_cvt_f32_u32_e32 v1, v2
	v_readlane_b32 s4, v254, 49
	v_readlane_b32 s5, v254, 50
	v_rcp_iflag_f32_e32 v1, v1
	s_nop 0
	v_mul_f32_e32 v1, 0x4f7ffffe, v1
	v_cvt_u32_f32_e32 v1, v1
	v_mul_lo_u32 v4, v4, v1
	v_mul_hi_u32 v4, v1, v4
	v_add_u32_e32 v1, v1, v4
	v_mul_hi_u32 v1, v3, v1
	v_mul_lo_u32 v4, v1, v2
	v_sub_u32_e32 v4, v3, v4
	v_cmp_ge_u32_e32 vcc, v4, v2
	v_add_u32_e32 v5, 1, v1
	v_add_u32_e32 v3, 1, v3
	v_cndmask_b32_e32 v1, v1, v5, vcc
	v_sub_u32_e32 v5, v4, v2
	v_cndmask_b32_e32 v4, v4, v5, vcc
	v_cmp_ge_u32_e32 vcc, v4, v2
	v_add_u32_e32 v4, 1, v1
	s_nop 0
	v_cndmask_b32_e32 v1, v1, v4, vcc
	v_mul_lo_u32 v4, v2, v1
	v_add_u32_e32 v2, v4, v2
	v_mov_b32_e32 v250, v2
	v_cmp_ne_u32_e32 vcc, v3, v2
	v_mov_b64_e32 v[2:3], s[4:5]
	s_and_saveexec_b64 s[4:5], vcc
	s_cbranch_execz .LBB0_1050
	v_readlane_b32 s8, v254, 47
	v_readlane_b32 s9, v254, 48
	s_mov_b64 s[10:11], 0
	s_nop 3
	global_load_dword v2, v115, s[8:9] sc1
	s_waitcnt vmcnt(0)
	v_cmp_lt_u32_e32 vcc, v2, v250
	s_and_saveexec_b64 s[8:9], vcc
	s_cbranch_execz .LBB0_1049
	s_mov_b32 s7, 1
	s_branch .LBB0_1042

.LBB0_1044:
	v_readlane_b32 s12, v254, 47
	v_readlane_b32 s13, v254, 48
	s_add_i32 s7, s7, 1
	s_mov_b64 s[40:41], -1
	s_nop 2
	global_load_dword v2, v115, s[12:13] sc1
	s_waitcnt vmcnt(0)
	v_cmp_ge_u32_e32 vcc, v2, v250
	s_orn2_b64 s[38:39], vcc, exec
	s_branch .LBB0_1041

.LBB0_1141:
	s_or_b64 exec, exec, s[10:11]
	s_waitcnt vmcnt(0)
	v_readfirstlane_b32 s7, v3
	v_sub_u32_e32 v4, 0, v2
	v_readlane_b32 s8, v254, 49
	v_add_u32_e32 v3, s7, v1
	v_cvt_f32_u32_e32 v1, v2
	v_readlane_b32 s9, v254, 50
	s_mov_b64 s[10:11], -1
	v_rcp_iflag_f32_e32 v1, v1
	s_nop 0
	v_mul_f32_e32 v1, 0x4f7ffffe, v1
	v_cvt_u32_f32_e32 v1, v1
	v_mul_lo_u32 v4, v4, v1
	v_mul_hi_u32 v4, v1, v4
	v_add_u32_e32 v1, v1, v4
	v_mul_hi_u32 v1, v3, v1
	v_mul_lo_u32 v4, v1, v2
	v_sub_u32_e32 v4, v3, v4
	v_cmp_ge_u32_e32 vcc, v4, v2
	v_add_u32_e32 v5, 1, v1
	v_add_u32_e32 v3, 1, v3
	v_cndmask_b32_e32 v1, v1, v5, vcc
	v_sub_u32_e32 v5, v4, v2
	v_cndmask_b32_e32 v4, v4, v5, vcc
	v_cmp_ge_u32_e32 vcc, v4, v2
	v_add_u32_e32 v4, 1, v1
	s_nop 0
	v_cndmask_b32_e32 v1, v1, v4, vcc
	v_mul_lo_u32 v4, v2, v1
	v_add_u32_e32 v2, v4, v2
	v_mov_b32_e32 v250, v2
	v_cmp_ne_u32_e32 vcc, v3, v2
	v_mov_b64_e32 v[2:3], s[8:9]
	s_and_saveexec_b64 s[8:9], vcc
	s_cbranch_execz .LBB0_1153
	v_readlane_b32 s10, v254, 47
	v_readlane_b32 s11, v254, 48
	s_mov_b64 s[26:27], 0
	s_nop 3
	global_load_dword v2, v115, s[10:11] sc1
	s_waitcnt vmcnt(0)
	v_cmp_lt_u32_e32 vcc, v2, v250
	s_and_saveexec_b64 s[10:11], vcc
	s_cbranch_execz .LBB0_1152
	s_mov_b32 s7, 1
	s_branch .LBB0_1145

.LBB0_1282:
	v_readlane_b32 s12, v254, 47
	v_readlane_b32 s13, v254, 48
	s_add_i32 s7, s7, 1
	s_mov_b64 s[38:39], -1
	s_nop 2
	global_load_dword v2, v115, s[12:13] sc1
	s_waitcnt vmcnt(0)
	v_cmp_ge_u32_e32 vcc, v2, v250
	s_orn2_b64 s[28:29], vcc, exec
	s_branch .LBB0_1279
